# baseline (speedup 1.0000x reference)
.LBB0_78:
	s_load_dwordx8 s[8:15], s[0:1], 0x0
	s_load_dwordx2 s[0:1], s[0:1], 0x28
	v_lshlrev_b32_e32 v2, 9, v0
	v_and_b32_e32 v13, 3, v0
	v_and_b32_e32 v2, 0x7800, v2
	v_mov_b32_e32 v3, 0
	v_lshl_or_b32 v12, s36, 2, v13
	s_waitcnt lgkmcnt(0)
	s_mov_b64 s[44:45], s[0:1]
	s_lshl_b32 s46, s33, 8
	v_add_u32_e32 v164, s46, v0
	v_lshrrev_b32_e32 v165, 2, v164
	v_min_u32_e32 v165, 0xc7, v165
	s_mul_i32 s46, s3, 0xc8
	v_add_lshl_u32 v165, v165, s46, 2
	global_load_dword v166, v165, s[8:9]
	global_load_dword v167, v165, s[10:11]
	v_lshl_add_u64 v[4:5], s[0:1], 0, v[2:3]
	s_lshl_b32 s0, s33, 7
	v_lshl_or_b32 v2, v12, 3, s0
	v_lshl_add_u64 v[10:11], v[4:5], 0, v[2:3]
	v_and_b32_e32 v160, 15, v0
	v_bfe_u32 v161, v0, 4, 2
	s_and_b32 s46, s36, 1
	s_lshl_b32 s46, s46, 5
	v_lshl_add_u32 v162, v161, 3, s46
	v_lshlrev_b32_e32 v162, 7, v162
	s_lshl_b32 s47, s33, 5
	s_lshr_b32 s46, s36, 1
	s_add_i32 s47, s47, s46
	v_lshl_add_u32 v163, v160, 1, s47
	v_add_lshl_u32 v162, v162, v163, 2
	global_load_dword v152, v162, s[44:45]
	global_load_dword v153, v162, s[44:45] offset:512
	global_load_dword v154, v162, s[44:45] offset:1024
	global_load_dword v155, v162, s[44:45] offset:1536
	global_load_dword v156, v162, s[44:45] offset:2048
	global_load_dword v157, v162, s[44:45] offset:2560
	global_load_dword v158, v162, s[44:45] offset:3072
	global_load_dword v159, v162, s[44:45] offset:3584
	s_bfe_u32 s5, s2, 0x30002
	s_mov_b32 s4, 2
	s_cmp_gt_u32 s5, 3
	v_lshlrev_b32_e32 v10, 2, v0
	s_cbranch_scc0 .LBB0_80
	v_and_b32_e32 v11, 16, v10
	v_lshl_or_b32 v14, s5, 5, v11
	s_cbranch_execz .LBB0_81
	s_branch .LBB0_82

.LBB0_86:
	s_or_b64 exec, exec, s[0:1]
	v_cmp_ne_u32_e32 vcc, 0, v14
	s_waitcnt lgkmcnt(0)
	s_barrier
	v_and_b32_e32 v168, 3, v164
	v_lshlrev_b32_e32 v168, 7, v168
	v_lshl_add_u32 v169, v166, 9, v168
	global_load_dword v171, v169, s[12:13]
	s_movk_i32 s46, 0x2710
	v_mad_u32_u24 v170, v167, s46, v166
	v_lshl_add_u32 v170, v170, 9, v168
	global_load_dword v172, v170, s[14:15]
	s_setprio 2
	v_and_b32_e32 v40, 15, v1
	v_lshrrev_b32_e32 v41, 4, v1
	s_and_b32 s44, s36, 1
	s_lshr_b32 s45, s36, 1
	s_mov_b32 s60, 0xffff
	s_mov_b32 s61, 0
	s_mov_b32 s62, 0xffff0000
	s_mov_b32 s63, 0
	s_mov_b32 s64, 0
	s_mov_b32 s65, 0xffff
	s_mov_b32 s66, 0
	s_mov_b32 s67, 0xffff0000
	v_cvt_pk_f16_f32 v2, v152, v153
	v_cvt_pk_f16_f32 v3, v154, v155
	v_cvt_pk_f16_f32 v4, v156, v157
	v_cvt_pk_f16_f32 v5, v158, v159
	s_lshl_b32 s46, s44, 3
	v_lshl_add_u32 v42, v41, 1, s46
	v_mul_u32_u24_e32 v32, 0x650, v42
	v_lshl_add_u32 v34, v40, 3, v32
	v_mul_u32_u24_e32 v33, 0x650, v40
	v_add_u32_e32 v33, 0x6500, v33
	s_lshl_b32 s47, s45, 1
	v_lshl_add_u32 v35, v40, 2, s47
	v_lshl_add_u32 v35, v41, 8, v35
	s_lshl_b32 s46, s3, 2
	s_add_i32 s46, s46, s33
	s_lshl_b32 s46, s46, 1
	s_add_i32 s46, s46, s44
	s_mul_i32 s46, s46, 0x3200
	s_add_u32 s68, s26, s46
	s_addc_u32 s69, s27, 0
	v_mov_b32_e32 v36, 0x14a00
